# attention tile loops with one signed-slope bias block and the edge mask out of line (no store deferral)
# baseline (speedup 1.0000x reference)
.LBB0_258:
	v_lshlrev_b32_e32 v10, 2, v174
	v_xor_b32_e32 v179, 0x80, v10
	v_max_f32_e32 v10, v0, v0
	v_max_f32_e32 v11, v21, v21
	v_max_f32_e32 v10, v11, v10
	v_max3_f32 v10, v10, v1, v18
	v_max3_f32 v10, v10, v19, v4
	v_max3_f32 v10, v10, v5, v6
	v_max3_f32 v10, v10, v7, v8
	v_max3_f32 v10, v10, v9, v2
	v_max3_f32 v10, v10, v3, v16
	v_max3_f32 v10, v10, v17, v37
	ds_bpermute_b32 v11, v179, v10
	v_mul_u32_u24_e32 v32, 0x410, v34
	s_add_i32 s31, 0, 0x12000
	v_lshl_add_u32 v12, s52, 1, v35
	v_add3_u32 v152, s31, v32, v12
	s_waitcnt lgkmcnt(0)
	v_max_f32_e32 v11, v11, v11
	v_max_f32_e32 v178, v10, v11
	v_sub_f32_e32 v0, v0, v178
	v_exp_f32_e32 v46, v0
	v_sub_f32_e32 v0, v1, v178
	v_exp_f32_e32 v47, v0
	v_sub_f32_e32 v0, v18, v178
	v_exp_f32_e32 v146, v0
	v_sub_f32_e32 v0, v19, v178
	v_exp_f32_e32 v147, v0
	v_sub_f32_e32 v0, v4, v178
	v_exp_f32_e32 v148, v0
	v_sub_f32_e32 v0, v5, v178
	v_exp_f32_e32 v149, v0
	v_sub_f32_e32 v0, v6, v178
	v_exp_f32_e32 v150, v0
	v_sub_f32_e32 v0, v7, v178
	ds_read_b128 v[4:7], v152
	ds_read_b128 v[38:41], v152 offset:32
	v_sub_f32_e32 v10, v21, v178
	v_exp_f32_e32 v33, v10
	v_exp_f32_e32 v151, v0
	v_sub_f32_e32 v0, v9, v178
	v_cvt_pk_bf16_f32 v21, v149, v150
	v_cvt_pk_bf16_f32 v20, v147, v148
	v_cvt_pk_bf16_f32 v19, v47, v146
	v_cvt_pk_bf16_f32 v18, v33, v46
	v_sub_f32_e32 v42, v8, v178
	v_exp_f32_e32 v153, v0
	v_sub_f32_e32 v43, v2, v178
	v_sub_f32_e32 v26, v3, v178
	ds_read_b128 v[22:25], v152 offset:33280
	s_waitcnt lgkmcnt(2)
	v_mfma_f32_32x32x16_bf16 v[0:15], v[4:7], v[18:21], 0
	v_sub_f32_e32 v44, v16, v178
	v_sub_f32_e32 v16, v17, v178
	v_exp_f32_e32 v155, v16
	v_sub_f32_e32 v16, v37, v178
	v_exp_f32_e32 v154, v26
	v_exp_f32_e32 v37, v16
	v_exp_f32_e32 v156, v44
	v_exp_f32_e32 v157, v43
	v_exp_f32_e32 v158, v42
	v_add_f32_e32 v33, 0, v33
	v_add_f32_e32 v33, v46, v33
	v_add_f32_e32 v33, v47, v33
	v_cvt_pk_bf16_f32 v45, v155, v37
	v_cvt_pk_bf16_f32 v44, v154, v156
	v_cvt_pk_bf16_f32 v43, v153, v157
	v_cvt_pk_bf16_f32 v42, v151, v158
	v_add_f32_e32 v33, v146, v33
	v_add_f32_e32 v33, v147, v33
	s_waitcnt lgkmcnt(1)
	v_mfma_f32_32x32x16_bf16 v[0:15], v[38:41], v[42:45], v[0:15]
	ds_read_b128 v[38:41], v152 offset:33312
	v_add_f32_e32 v33, v148, v33
	v_add_f32_e32 v33, v149, v33
	v_add_f32_e32 v33, v150, v33
	v_add_f32_e32 v33, v151, v33
	v_add_f32_e32 v33, v158, v33
	v_add_f32_e32 v33, v153, v33
	s_waitcnt lgkmcnt(1)
	v_mfma_f32_32x32x16_bf16 v[16:31], v[22:25], v[18:21], 0
	v_add_f32_e32 v33, v157, v33
	v_add_f32_e32 v33, v154, v33
	v_add_f32_e32 v33, v156, v33
	v_readlane_b32 s0, v254, 59
	v_add_f32_e32 v33, v155, v33
	s_add_i32 s0, s0, s51
	v_add_f32_e32 v180, v37, v33
	s_waitcnt lgkmcnt(0)
	v_mfma_f32_32x32x16_bf16 v[16:31], v[38:41], v[42:45], v[16:31]
	v_add_u32_e32 v33, s0, v34
	v_subrev_u32_e32 v33, s50, v33
	s_movk_i32 s0, 0x90
	v_mul_lo_u32 v33, v33, s0
	s_lshl_b32 s0, s51, 1
	v_add3_u32 v32, v32, v35, s0
	s_lshl_b32 s0, s50, 1
	v_xor_b32_e32 v172, 0x80000000, v170
	v_subrev_u32_e32 v32, s0, v32
	v_readlane_b32 s0, v255, 8
	v_readlane_b32 s52, v254, 21
	v_mov_b32_e32 v171, v170
	s_sub_i32 s33, s33, 64
	s_sub_i32 s38, s21, 31
	v_mov_b32_e32 v173, v172
	v_add3_u32 v181, v33, v35, 0
	v_add_u32_e32 v182, s0, v32
	v_add_u32_e32 v182, 0x12140, v182
	v_subrev_u32_e32 v183, 64, v36
	v_cvt_f32_i32_e32 v185, v183
	s_mov_b32 s39, 0
	s_movk_i32 s40, 0xfec0
	v_readlane_b32 s53, v254, 22
	v_mov_b32_e32 v204, v170
	v_mov_b32_e32 v205, v170
	s_branch .LBB0_261

.LBB0_261:
	s_cmpk_eq_i32 s40, 0xff40
	s_cbranch_scc1 .Lflip_d
	s_cmpk_lt_i32 s33, 0xffe1
	s_cselect_b64 s[0:1], -1, 0
	s_cmp_ge_i32 s33, s21
	s_cselect_b64 s[36:37], -1, 0
	s_or_b64 s[0:1], s[0:1], s[36:37]
	s_and_b64 vcc, exec, s[0:1]
	s_cbranch_vccnz .LBB0_260
	ds_read_b128 v[166:169], v181
	ds_read_b128 v[162:165], v181 offset:32
	ds_read_b128 v[158:161], v181 offset:64
	ds_read_b128 v[154:157], v181 offset:96
	v_add_u32_e32 v184, s40, v182
	ds_read_b128 v[150:153], v184
	ds_read_b128 v[146:149], v184 offset:33280
	v_fma_f32 v46, v204, v185, -v178
	v_fma_f32 v32, 0, v204, v46
	v_add_f32_e32 v33, v204, v46
	v_pk_fma_f32 v[34:35], v[204:205], s[28:29], v[46:47] op_sel_hi:[1,1,0]
	v_pk_fma_f32 v[36:37], v[204:205], s[84:85], v[46:47] op_sel_hi:[1,1,0]
	v_pk_fma_f32 v[38:39], v[204:205], s[82:83], v[46:47] op_sel_hi:[1,1,0]
	v_pk_fma_f32 v[40:41], v[204:205], s[26:27], v[46:47] op_sel_hi:[1,1,0]
	v_pk_fma_f32 v[42:43], v[204:205], s[24:25], v[46:47] op_sel_hi:[1,1,0]
	v_pk_fma_f32 v[44:45], v[204:205], s[86:87], v[46:47] op_sel_hi:[1,1,0]
	v_pk_fma_f32 v[46:47], v[204:205], s[2:3], v[46:47] op_sel_hi:[1,1,0]
.LBB0_267:
	s_and_b32 s41, s39, 3
	s_cmp_lt_i32 s33, 0
	s_cselect_b64 s[0:1], -1, 0
	s_cmp_ge_i32 s33, s38
	s_cselect_b64 s[36:37], -1, 0
	s_cmp_eq_u32 s41, 0
	s_cselect_b64 s[50:51], -1, 0
	s_or_b64 s[0:1], s[50:51], s[0:1]
	s_or_b64 s[0:1], s[0:1], s[36:37]
	s_andn2_b64 vcc, exec, s[0:1]
	s_cbranch_vccz .Lmask_d

.Lmask_d:
	v_cmp_nge_f32_e32 vcc, v185, v177
	v_cmp_nle_f32_e64 s[36:37], v185, v176
	s_or_b64 vcc, vcc, s[36:37]
	v_add_f32_e32 v186, 1.0, v185
	v_cndmask_b32_e32 v32, v32, v237, vcc
	v_cmp_nge_f32_e32 vcc, v186, v177
	v_cmp_nle_f32_e64 s[36:37], v186, v176
	s_or_b64 vcc, vcc, s[36:37]
	v_add_f32_e32 v186, 2.0, v185
	v_cndmask_b32_e32 v33, v33, v237, vcc
	v_cmp_nge_f32_e32 vcc, v186, v177
	v_cmp_nle_f32_e64 s[36:37], v186, v176
	s_or_b64 vcc, vcc, s[36:37]
	v_add_f32_e32 v186, 0x40400000, v185
	v_cndmask_b32_e32 v34, v34, v237, vcc
	v_cmp_nge_f32_e32 vcc, v186, v177
	v_cmp_nle_f32_e64 s[36:37], v186, v176
	s_or_b64 vcc, vcc, s[36:37]
	v_add_f32_e32 v186, 0x41000000, v185
	v_cndmask_b32_e32 v35, v35, v237, vcc
	v_cmp_nge_f32_e32 vcc, v186, v177
	v_cmp_nle_f32_e64 s[36:37], v186, v176
	s_or_b64 vcc, vcc, s[36:37]
	v_add_f32_e32 v186, 0x41100000, v185
	v_cndmask_b32_e32 v36, v36, v237, vcc
	v_cmp_nge_f32_e32 vcc, v186, v177
	v_cmp_nle_f32_e64 s[36:37], v186, v176
	s_or_b64 vcc, vcc, s[36:37]
	v_add_f32_e32 v186, 0x41200000, v185
	v_cndmask_b32_e32 v37, v37, v237, vcc
	v_cmp_nge_f32_e32 vcc, v186, v177
	v_cmp_nle_f32_e64 s[36:37], v186, v176
	s_or_b64 vcc, vcc, s[36:37]
	v_add_f32_e32 v186, 0x41300000, v185
	v_cndmask_b32_e32 v38, v38, v237, vcc
	v_cmp_nge_f32_e32 vcc, v186, v177
	v_cmp_nle_f32_e64 s[36:37], v186, v176
	s_or_b64 vcc, vcc, s[36:37]
	v_add_f32_e32 v186, 0x41800000, v185
	v_cndmask_b32_e32 v39, v39, v237, vcc
	v_cmp_nge_f32_e32 vcc, v186, v177
	v_cmp_nle_f32_e64 s[36:37], v186, v176
	s_or_b64 vcc, vcc, s[36:37]
	v_add_f32_e32 v186, 0x41880000, v185
	v_cndmask_b32_e32 v40, v40, v237, vcc
	v_cmp_nge_f32_e32 vcc, v186, v177
	v_cmp_nle_f32_e64 s[36:37], v186, v176
	s_or_b64 vcc, vcc, s[36:37]
	v_add_f32_e32 v186, 0x41900000, v185
	v_cndmask_b32_e32 v41, v41, v237, vcc
	v_cmp_nge_f32_e32 vcc, v186, v177
	v_cmp_nle_f32_e64 s[36:37], v186, v176
	s_or_b64 vcc, vcc, s[36:37]
	v_add_f32_e32 v186, 0x41980000, v185
	v_cndmask_b32_e32 v42, v42, v237, vcc
	v_cmp_nge_f32_e32 vcc, v186, v177
	v_cmp_nle_f32_e64 s[36:37], v186, v176
	s_or_b64 vcc, vcc, s[36:37]
	v_add_f32_e32 v186, 0x41c00000, v185
	v_cndmask_b32_e32 v43, v43, v237, vcc
	v_cmp_nge_f32_e32 vcc, v186, v177
	v_cmp_nle_f32_e64 s[36:37], v186, v176
	s_or_b64 vcc, vcc, s[36:37]
	v_add_f32_e32 v186, 0x41c80000, v185
	v_cndmask_b32_e32 v44, v44, v237, vcc
	v_cmp_nge_f32_e32 vcc, v186, v177
	v_cmp_nle_f32_e64 s[36:37], v186, v176
	s_or_b64 vcc, vcc, s[36:37]
	v_add_f32_e32 v186, 0x41d00000, v185
	v_cndmask_b32_e32 v45, v45, v237, vcc
	v_cmp_nge_f32_e32 vcc, v186, v177
	v_cmp_nle_f32_e64 s[36:37], v186, v176
	s_or_b64 vcc, vcc, s[36:37]
	v_add_f32_e32 v186, 0x41d80000, v185
	v_cndmask_b32_e32 v46, v46, v237, vcc
	v_cmp_nge_f32_e32 vcc, v186, v177
	v_cmp_nle_f32_e64 s[36:37], v186, v176
	s_or_b64 vcc, vcc, s[36:37]
	v_cndmask_b32_e32 v47, v47, v237, vcc
	s_branch .LBB0_269
.Lflip_d:
	v_mov_b32_e32 v204, v172
	v_mov_b32_e32 v205, v172
	s_branch .LBB0_260

.LBB0_334:
	v_max_f32_e32 v10, v0, v0
	v_max_f32_e32 v11, v20, v20
	v_max_f32_e32 v10, v11, v10
	v_max3_f32 v10, v10, v1, v2
	v_max3_f32 v10, v10, v3, v4
	v_max3_f32 v10, v10, v5, v6
	v_max3_f32 v10, v10, v7, v8
	v_max3_f32 v10, v10, v9, v16
	v_max3_f32 v10, v10, v17, v18
	v_max3_f32 v10, v10, v19, v21
	ds_bpermute_b32 v11, v243, v10
	v_xor_b32_e32 v226, 0x80000000, v224
	v_mov_b32_e32 v225, v224
	v_mov_b32_e32 v227, v226
	s_mov_b32 s19, 0
	s_waitcnt lgkmcnt(0)
	v_max_f32_e32 v11, v11, v11
	v_max_f32_e32 v249, v10, v11
	v_sub_f32_e32 v0, v0, v249
	v_exp_f32_e32 v37, v0
	v_sub_f32_e32 v0, v2, v249
	v_exp_f32_e32 v39, v0
	v_sub_f32_e32 v0, v3, v249
	v_exp_f32_e32 v40, v0
	v_sub_f32_e32 v0, v4, v249
	v_exp_f32_e32 v41, v0
	v_sub_f32_e32 v0, v5, v249
	v_sub_f32_e32 v10, v20, v249
	v_sub_f32_e32 v1, v1, v249
	v_exp_f32_e32 v42, v0
	v_sub_f32_e32 v0, v6, v249
	v_exp_f32_e32 v36, v10
	v_exp_f32_e32 v38, v1
	v_exp_f32_e32 v43, v0
	v_sub_f32_e32 v33, v16, v249
	v_sub_f32_e32 v16, v17, v249
	v_sub_f32_e32 v0, v7, v249
	v_exp_f32_e32 v46, v16
	v_sub_f32_e32 v16, v19, v249
	v_exp_f32_e32 v44, v0
	v_sub_f32_e32 v0, v9, v249
	v_cvt_pk_bf16_f32 v25, v42, v43
	v_cvt_pk_bf16_f32 v24, v40, v41
	v_cvt_pk_bf16_f32 v23, v38, v39
	v_cvt_pk_bf16_f32 v22, v36, v37
	v_exp_f32_e32 v47, v16
	v_sub_f32_e32 v16, v21, v249
	v_sub_f32_e32 v32, v8, v249
	v_exp_f32_e32 v45, v0
	v_mfma_f32_32x32x16_bf16 v[0:15], v[162:165], v[22:25], 0
	v_sub_f32_e32 v34, v18, v249
	v_exp_f32_e32 v178, v16
	v_exp_f32_e32 v179, v34
	v_exp_f32_e32 v180, v33
	v_exp_f32_e32 v181, v32
	v_cvt_pk_bf16_f32 v35, v47, v178
	v_cvt_pk_bf16_f32 v34, v46, v179
	v_mfma_f32_32x32x16_bf16 v[16:31], v[170:173], v[22:25], 0
	v_cvt_pk_bf16_f32 v33, v45, v180
	v_cvt_pk_bf16_f32 v32, v44, v181
	s_movk_i32 s20, 0xfdc0
	s_mov_b32 s21, s5
	v_cvt_f32_i32_e32 v234, v247
	v_mov_b32_e32 v252, v245
	v_mfma_f32_32x32x16_bf16 v[0:15], v[166:169], v[32:35], v[0:15]
	v_mfma_f32_32x32x16_bf16 v[16:31], v[174:177], v[32:35], v[16:31]
	v_add_f32_e32 v32, 0, v36
	v_add_f32_e32 v32, v37, v32
	v_add_f32_e32 v32, v38, v32
	v_add_f32_e32 v32, v39, v32
	v_add_f32_e32 v32, v40, v32
	v_add_f32_e32 v32, v41, v32
	v_add_f32_e32 v32, v42, v32
	v_add_f32_e32 v32, v43, v32
	v_add_f32_e32 v32, v44, v32
	v_add_f32_e32 v32, v181, v32
	v_add_f32_e32 v32, v45, v32
	v_add_f32_e32 v32, v180, v32
	v_add_f32_e32 v32, v46, v32
	v_add_f32_e32 v32, v179, v32
	v_add_f32_e32 v32, v47, v32
	v_add_f32_e32 v250, v178, v32
	v_mov_b32_e32 v204, v224
	v_mov_b32_e32 v205, v224
	s_branch .LBB0_337

.LBB0_337:
	s_cmpk_eq_i32 s20, 0xfec0
	s_cbranch_scc1 .Lflip_w
	s_add_i32 s0, s21, 31
	s_cmpk_gt_u32 s0, 0x81e
	s_cbranch_scc1 .LBB0_336
	ds_read_b128 v[198:201], v252
	ds_read_b128 v[194:197], v252 offset:32
	ds_read_b128 v[190:193], v252 offset:64
	ds_read_b128 v[186:189], v252 offset:96
	v_add_u32_e32 v235, s20, v246
	ds_read_b128 v[182:185], v235
	ds_read_b128 v[178:181], v235 offset:33280
	v_fma_f32 v46, v204, v234, -v249
	v_fma_f32 v32, 0, v204, v46
	v_add_f32_e32 v33, v204, v46
	v_pk_fma_f32 v[34:35], v[204:205], s[28:29], v[46:47] op_sel_hi:[1,1,0]
	v_pk_fma_f32 v[36:37], v[204:205], s[84:85], v[46:47] op_sel_hi:[1,1,0]
	v_pk_fma_f32 v[38:39], v[204:205], s[82:83], v[46:47] op_sel_hi:[1,1,0]
	v_pk_fma_f32 v[40:41], v[204:205], s[26:27], v[46:47] op_sel_hi:[1,1,0]
	v_pk_fma_f32 v[42:43], v[204:205], s[24:25], v[46:47] op_sel_hi:[1,1,0]
	v_pk_fma_f32 v[44:45], v[204:205], s[86:87], v[46:47] op_sel_hi:[1,1,0]
	v_pk_fma_f32 v[46:47], v[204:205], s[2:3], v[46:47] op_sel_hi:[1,1,0]
.LBB0_343:
	s_and_b32 s22, s19, 7
	s_cmpk_lt_u32 s21, 0x800
	s_cselect_b64 s[0:1], -1, 0
	s_cmp_lg_u32 s22, 0
	s_cselect_b64 s[30:31], -1, 0
	s_and_b64 s[0:1], s[30:31], s[0:1]
	s_and_b64 vcc, exec, s[0:1]
	s_cbranch_vccz .Lmask_w

.Lmask_w:
	v_cmp_nge_f32_e32 vcc, v234, v241
	v_cmp_nle_f32_e64 s[68:69], v234, v242
	s_or_b64 vcc, vcc, s[68:69]
	v_add_f32_e32 v202, 1.0, v234
	v_cndmask_b32_e32 v32, v32, v237, vcc
	v_cmp_nge_f32_e32 vcc, v202, v241
	v_cmp_nle_f32_e64 s[68:69], v202, v242
	s_or_b64 vcc, vcc, s[68:69]
	v_add_f32_e32 v202, 2.0, v234
	v_cndmask_b32_e32 v33, v33, v237, vcc
	v_cmp_nge_f32_e32 vcc, v202, v241
	v_cmp_nle_f32_e64 s[68:69], v202, v242
	s_or_b64 vcc, vcc, s[68:69]
	v_add_f32_e32 v202, 0x40400000, v234
	v_cndmask_b32_e32 v34, v34, v237, vcc
	v_cmp_nge_f32_e32 vcc, v202, v241
	v_cmp_nle_f32_e64 s[68:69], v202, v242
	s_or_b64 vcc, vcc, s[68:69]
	v_add_f32_e32 v202, 0x41000000, v234
	v_cndmask_b32_e32 v35, v35, v237, vcc
	v_cmp_nge_f32_e32 vcc, v202, v241
	v_cmp_nle_f32_e64 s[68:69], v202, v242
	s_or_b64 vcc, vcc, s[68:69]
	v_add_f32_e32 v202, 0x41100000, v234
	v_cndmask_b32_e32 v36, v36, v237, vcc
	v_cmp_nge_f32_e32 vcc, v202, v241
	v_cmp_nle_f32_e64 s[68:69], v202, v242
	s_or_b64 vcc, vcc, s[68:69]
	v_add_f32_e32 v202, 0x41200000, v234
	v_cndmask_b32_e32 v37, v37, v237, vcc
	v_cmp_nge_f32_e32 vcc, v202, v241
	v_cmp_nle_f32_e64 s[68:69], v202, v242
	s_or_b64 vcc, vcc, s[68:69]
	v_add_f32_e32 v202, 0x41300000, v234
	v_cndmask_b32_e32 v38, v38, v237, vcc
	v_cmp_nge_f32_e32 vcc, v202, v241
	v_cmp_nle_f32_e64 s[68:69], v202, v242
	s_or_b64 vcc, vcc, s[68:69]
	v_add_f32_e32 v202, 0x41800000, v234
	v_cndmask_b32_e32 v39, v39, v237, vcc
	v_cmp_nge_f32_e32 vcc, v202, v241
	v_cmp_nle_f32_e64 s[68:69], v202, v242
	s_or_b64 vcc, vcc, s[68:69]
	v_add_f32_e32 v202, 0x41880000, v234
	v_cndmask_b32_e32 v40, v40, v237, vcc
	v_cmp_nge_f32_e32 vcc, v202, v241
	v_cmp_nle_f32_e64 s[68:69], v202, v242
	s_or_b64 vcc, vcc, s[68:69]
	v_add_f32_e32 v202, 0x41900000, v234
	v_cndmask_b32_e32 v41, v41, v237, vcc
	v_cmp_nge_f32_e32 vcc, v202, v241
	v_cmp_nle_f32_e64 s[68:69], v202, v242
	s_or_b64 vcc, vcc, s[68:69]
	v_add_f32_e32 v202, 0x41980000, v234
	v_cndmask_b32_e32 v42, v42, v237, vcc
	v_cmp_nge_f32_e32 vcc, v202, v241
	v_cmp_nle_f32_e64 s[68:69], v202, v242
	s_or_b64 vcc, vcc, s[68:69]
	v_add_f32_e32 v202, 0x41c00000, v234
	v_cndmask_b32_e32 v43, v43, v237, vcc
	v_cmp_nge_f32_e32 vcc, v202, v241
	v_cmp_nle_f32_e64 s[68:69], v202, v242
	s_or_b64 vcc, vcc, s[68:69]
	v_add_f32_e32 v202, 0x41c80000, v234
	v_cndmask_b32_e32 v44, v44, v237, vcc
	v_cmp_nge_f32_e32 vcc, v202, v241
	v_cmp_nle_f32_e64 s[68:69], v202, v242
	s_or_b64 vcc, vcc, s[68:69]
	v_add_f32_e32 v202, 0x41d00000, v234
	v_cndmask_b32_e32 v45, v45, v237, vcc
	v_cmp_nge_f32_e32 vcc, v202, v241
	v_cmp_nle_f32_e64 s[68:69], v202, v242
	s_or_b64 vcc, vcc, s[68:69]
	v_add_f32_e32 v202, 0x41d80000, v234
	v_cndmask_b32_e32 v46, v46, v237, vcc
	v_cmp_nge_f32_e32 vcc, v202, v241
	v_cmp_nle_f32_e64 s[68:69], v202, v242
	s_or_b64 vcc, vcc, s[68:69]
	v_cndmask_b32_e32 v47, v47, v237, vcc
	s_branch .LBB0_345
.Lflip_w:
	v_mov_b32_e32 v204, v226
	v_mov_b32_e32 v205, v226
	s_branch .LBB0_336
